# stack11: stack9 + GLA-finish items start at wave*256+block (one 9-item and one 8-item wave per SIMD instead of 9-item blocks 0..127)
# speedup vs baseline: 1.0044x; 1.0044x over previous
.LBB0_814:
	s_cmp_lt_i32 s86, 6
	s_cselect_b64 s[0:1], -1, 0
	s_and_b64 s[4:5], s[0:1], s[4:5]
	s_andn2_b64 vcc, exec, s[4:5]
	s_cbranch_vccnz .LBB0_818
	v_readlane_b32 s0, v255, 25
	s_cmpk_gt_i32 s0, 0x43ff
	v_readlane_b32 s1, v255, 26
	s_cbranch_scc1 .LBB0_818
	s_add_u32 s6, s84, 0x36c00000
	s_addc_u32 s7, s85, 0
	s_add_u32 s8, s84, 0x3b000000
	s_addc_u32 s9, s85, 0
	s_add_u32 s10, s84, 0x25300000
	v_readlane_b32 s0, v255, 25
	s_addc_u32 s11, s85, 0
	v_readlane_b32 s1, v255, 26
	s_mov_b32 s20, s0
	s_cmp_lg_u32 s92, 0x800
	s_cbranch_scc1 .Lp5map_skip
	s_and_b32 s20, s0, 7
	s_lshl_b32 s20, s20, 8
	s_lshr_b32 s21, s0, 3
	s_or_b32 s20, s20, s21
.Lp5map_skip:
	s_ashr_i32 s21, s0, 31
	s_lshl_b64 s[0:1], s[20:21], 12
	s_add_u32 s0, s84, s0
	s_addc_u32 s1, s85, s1
	s_add_u32 s12, s0, 0x31f00000
	v_readlane_b32 s0, v255, 25
	s_addc_u32 s13, s1, 0
	s_nop 0
	s_waitcnt vmcnt(0)
	v_mbcnt_lo_u32_b32 v2, -1, 0
	v_mbcnt_hi_u32_b32 v49, -1, v2
	v_writelane_b32 v255, s1, 26
	s_ashr_i32 s93, s92, 31
	v_readlane_b32 s36, v255, 4
	v_and_b32_e32 v2, 64, v49
	v_readlane_b32 s42, v255, 10
	v_readlane_b32 s43, v255, 11
	v_lshlrev_b32_e32 v48, 3, v1
	s_lshl_b64 s[14:15], s[92:93], 12
	s_lshl_b64 s[16:17], s[20:21], 11
	s_lshl_b64 s[18:19], s[92:93], 11
	v_add_u32_e32 v50, 64, v2
	v_xor_b32_e32 v51, 1, v49
	v_xor_b32_e32 v52, 2, v49
	v_xor_b32_e32 v53, 4, v49
	v_xor_b32_e32 v54, 8, v49
	v_xor_b32_e32 v55, 16, v49
	v_xor_b32_e32 v56, 32, v49
	v_mov_b32_e32 v57, 0x3727c5ac
	s_mov_b32 s2, 0xf800000
	v_mov_b32_e32 v58, 0x260
	s_mov_b64 s[22:23], s[42:43]
	v_readlane_b32 s37, v255, 5
	v_readlane_b32 s38, v255, 6
	v_readlane_b32 s39, v255, 7
	v_readlane_b32 s40, v255, 8
	v_readlane_b32 s41, v255, 9
	v_readlane_b32 s44, v255, 12
	v_readlane_b32 s45, v255, 13
	v_readlane_b32 s46, v255, 14
	v_readlane_b32 s47, v255, 15
	v_readlane_b32 s48, v255, 16
	v_readlane_b32 s49, v255, 17
	v_readlane_b32 s50, v255, 18
	v_readlane_b32 s51, v255, 19
